# v4 plus: mLSTM chunk-top waits no longer drain the h stores; out_proj and MoE-down epilogue loads de-serialised
# speedup vs baseline: 1.0429x; 1.0033x over previous
.Lpp_ropedone_kk_8:
	v_cvt_pk_bf16_f32 v156, v156, v157
	v_cvt_pk_bf16_f32 v157, v158, v159
	v_cvt_pk_bf16_f32 v158, v160, v161
	v_cvt_pk_bf16_f32 v159, v162, v163
	s_mov_b64 exec, 0xffffffff
	global_store_dwordx4 v4, v[156:159], s[28:29]
	s_mov_b64 exec, s[66:67]
	global_store_dwordx4 v4, v[156:159], s[30:31]
	s_mov_b64 exec, -1
	v_lshlrev_b32_e32 v148, 16, v116
	v_and_b32_e32 v149, 0xffff0000, v116
	v_lshlrev_b32_e32 v150, 16, v117
	v_and_b32_e32 v151, 0xffff0000, v117
	v_lshlrev_b32_e32 v152, 16, v118
	v_and_b32_e32 v153, 0xffff0000, v118
	v_lshlrev_b32_e32 v154, 16, v119
	v_and_b32_e32 v155, 0xffff0000, v119
	v_mul_f32_e32 v164, v148, v148
	v_fmac_f32_e32 v164, v149, v149
	v_fmac_f32_e32 v164, v150, v150
	v_fmac_f32_e32 v164, v151, v151
	v_fmac_f32_e32 v164, v152, v152
	v_fmac_f32_e32 v164, v153, v153
	v_fmac_f32_e32 v164, v154, v154
	v_fmac_f32_e32 v164, v155, v155
	v_mul_f32_e32 v148, v148, v28
	v_mul_f32_e32 v149, v149, v29
	v_add_f32_dpp v164, v164, v164 quad_perm:[1,0,3,2] row_mask:0xf bank_mask:0xf
	v_mul_f32_e32 v150, v150, v30
	v_mul_f32_e32 v151, v151, v31
	v_add_f32_dpp v164, v164, v164 quad_perm:[2,3,0,1] row_mask:0xf bank_mask:0xf
	v_mul_f32_e32 v152, v152, v32
	v_mul_f32_e32 v153, v153, v33
	v_add_f32_dpp v164, v164, v164 row_half_mirror row_mask:0xf bank_mask:0xf
	v_mul_f32_e32 v154, v154, v34
	v_mul_f32_e32 v155, v155, v35
	v_add_f32_dpp v164, v164, v164 row_mirror row_mask:0xf bank_mask:0xf
	s_nop 0
	v_readlane_b32 s0, v164, 0
	v_readlane_b32 s1, v164, 16
	v_readlane_b32 s2, v164, 32
	v_readlane_b32 s3, v164, 48
	s_nop 1
	v_mov_b32_e32 v166, s0
	v_add_f32_e32 v166, s1, v166
	v_add_f32_e32 v166, s2, v166
	v_add_f32_e32 v166, s3, v166
	v_add_f32_e32 v166, 0x3a0637bd, v166
	v_rsq_f32_e32 v165, v166
	s_nop 0
	v_mul_f32_e32 v148, v148, v165
	v_mul_f32_e32 v149, v149, v165
	v_mul_f32_e32 v150, v150, v165
	v_mul_f32_e32 v151, v151, v165
	v_mul_f32_e32 v152, v152, v165
	v_mul_f32_e32 v153, v153, v165
	v_mul_f32_e32 v154, v154, v165
	v_mul_f32_e32 v155, v155, v165
	v_cvt_pk_bf16_f32 v156, v148, v149
	v_cvt_pk_bf16_f32 v157, v150, v151
	v_cvt_pk_bf16_f32 v158, v152, v153
	v_cvt_pk_bf16_f32 v159, v154, v155
	global_store_dwordx4 v4, v[156:159], s[34:35]
	v_add_f32_e32 v176, v136, v11
	v_mul_f32_e64 v177, |v176|, s47
	v_exp_f32_e32 v177, v177
	s_nop 0
	v_add_f32_e32 v178, 1.0, v177
	v_add_f32_e32 v179, -1.0, v178
	v_log_f32_e32 v180, v178
	v_rcp_f32_e32 v181, v179
	v_cmp_eq_f32_e32 vcc, 0, v179
	s_nop 0
	v_mul_f32_e32 v181, v177, v181
	s_nop 0
	v_cndmask_b32_e64 v181, v181, 1.0, vcc
	v_mul_f32_e32 v180, 0x3f317218, v180
	v_mul_f32_e32 v180, v180, v181
	v_min_f32_e32 v177, 0, v176
	v_sub_f32_e32 v177, v177, v180
	v_cndmask_b32_e64 v177, v176, v177, s[68:69]
	s_mov_b64 exec, 0xffff
	global_store_dword v8, v177, s[44:45]
	s_mov_b64 exec, -1
	v_readlane_b32 s0, v255, 22
	s_add_i32 s2, s0, 4
	v_readlane_b32 s0, v251, 39
	v_readlane_b32 s1, v251, 40
	s_cmp_ge_i32 s2, s1
	s_cbranch_scc1 .LBB0_6363
	s_waitcnt vmcnt(0)
	s_barrier
	s_mov_b64 s[0:1], exec
	v_readlane_b32 s4, v251, 37
	v_readlane_b32 s5, v251, 38
	s_and_b64 s[4:5], s[0:1], s[4:5]
	s_mov_b64 exec, s[4:5]
	s_cbranch_execz .LBB0_6362
	v_readlane_b32 s3, v255, 11
	s_waitcnt vmcnt(0) expcnt(0) lgkmcnt(0)
	s_nop 0
	v_mov_b32_e32 v1, s3
	ds_read_b32 v4, v1
	v_readlane_b32 s3, v255, 12
	s_waitcnt lgkmcnt(0)
	v_cmp_ne_u32_e32 vcc, 0, v4
	v_mov_b32_e32 v1, s3
	ds_read_b32 v2, v1
	s_cbranch_vccnz .LBB0_6326
	v_readlane_b32 s20, v251, 0
	v_readlane_b32 s21, v251, 1
	s_load_dwordx2 s[4:5], s[20:21], 0x4
	v_readlane_b32 s3, v251, 2
	s_mov_b32 s6, 1
	s_waitcnt lgkmcnt(0)
	s_mul_i32 s3, s4, s3
	s_mul_i32 s3, s3, s5
	s_branch .LBB0_6314

.Lmp_ropedone_k8:
	v_cvt_pk_bf16_f32 v100, v100, v101
	v_cvt_pk_bf16_f32 v101, v102, v103
	v_cvt_pk_bf16_f32 v102, v104, v105
	v_cvt_pk_bf16_f32 v103, v106, v107
	v_cvt_pk_bf16_f32 v118, v118, v119
	v_cvt_pk_bf16_f32 v119, v120, v121
	global_store_dwordx4 v4, v[100:103], s[30:31]
	global_store_dwordx2 v5, v[118:119], s[30:31]
	s_nop 1
	v_readlane_b32 s0, v255, 22
	s_add_i32 s2, s0, 6
	v_readlane_b32 s0, v251, 39
	v_readlane_b32 s1, v251, 40
	s_cmp_ge_i32 s2, s1
	s_cbranch_scc1 .LBB0_6626
	s_waitcnt vmcnt(0)
	s_waitcnt lgkmcnt(0)
	s_barrier
	s_mov_b64 s[0:1], exec
	v_readlane_b32 s4, v251, 37
	v_readlane_b32 s5, v251, 38
	s_and_b64 s[4:5], s[0:1], s[4:5]
	s_mov_b64 exec, s[4:5]
	s_cbranch_execz .LBB0_6625
	v_readlane_b32 s3, v255, 11
	s_waitcnt vmcnt(0) expcnt(0) lgkmcnt(0)
	s_nop 0
	v_mov_b32_e32 v1, s3
	ds_read_b32 v4, v1
	v_readlane_b32 s3, v255, 12
	s_waitcnt lgkmcnt(0)
	v_cmp_ne_u32_e32 vcc, 0, v4
	v_mov_b32_e32 v1, s3
	ds_read_b32 v2, v1
	s_cbranch_vccnz .LBB0_6589
	v_readlane_b32 s20, v251, 0
	v_readlane_b32 s21, v251, 1
	s_load_dwordx2 s[4:5], s[20:21], 0x4
	v_readlane_b32 s3, v251, 2
	s_mov_b32 s6, 1
	s_waitcnt lgkmcnt(0)
	s_mul_i32 s3, s4, s3
	s_mul_i32 s3, s3, s5
	s_branch .LBB0_6577

.LBB0_6641:
	s_or_b64 exec, exec, s[0:1]
	s_movk_i32 s0, 0x80
	v_cmp_gt_i32_e64 s[38:39], s0, v1
	s_and_saveexec_b64 s[0:1], s[38:39]
	v_add_u32_e32 v2, 0x20c00, v2
	ds_write_b32 v2, v3
	s_or_b64 exec, exec, s[0:1]
	s_add_u32 s2, s60, 0x41490000
	s_addc_u32 s3, s61, 0
	v_readlane_b32 s0, v253, 45
	s_add_u32 s4, s60, s0
	s_addc_u32 s5, s61, 0
	v_readlane_b32 s0, v254, 37
	s_add_u32 s0, s2, s0
	v_readlane_b32 s1, v254, 36
	s_addc_u32 s1, s3, s1
	v_readlane_b32 s8, v254, 44
	s_add_u32 s0, s0, s8
	v_lshlrev_b32_e32 v2, 4, v1
	v_ashrrev_i32_e32 v31, 4, v1
	s_addc_u32 s1, s1, 0
	v_and_b32_e32 v2, 0xf0, v2
	v_lshl_add_u64 v[4:5], s[0:1], 0, v[2:3]
	s_movk_i32 s9, 0x2400
	v_add_u32_e32 v6, 32, v31
	v_mad_i64_i32 v[16:17], s[0:1], v31, s9, v[4:5]
	v_mad_i64_i32 v[24:25], s[0:1], v6, s9, v[4:5]
	v_mad_i64_i32 v[50:51], s[0:1], v6, s9, 0
	global_load_dwordx4 v[4:7], v[16:17], off
	global_load_dwordx4 v[8:11], v[16:17], off offset:1024
	global_load_dwordx4 v[12:15], v[24:25], off
	s_nop 0
	global_load_dwordx4 v[16:19], v[16:17], off offset:2048
	s_nop 0
	global_load_dwordx4 v[20:23], v[24:25], off offset:1024
	s_nop 0
	global_load_dwordx4 v[24:27], v[24:25], off offset:2048
	v_mad_i64_i32 v[48:49], s[0:1], v31, s9, 0
	s_add_u32 s0, s2, s8
	v_lshrrev_b32_e32 v29, 4, v28
	s_addc_u32 s1, s3, 0
	v_bfe_u32 v32, v1, 2, 2
	v_lshlrev_b32_e32 v33, 3, v29
	v_lshl_add_u64 v[52:53], s[0:1], 0, v[2:3]
	s_add_u32 s0, s4, s8
	v_or_b32_e32 v32, v33, v32
	v_lshlrev_b32_e32 v34, 2, v1
	s_addc_u32 s1, s5, 0
	s_ashr_i32 s3, s24, 7
	v_mul_u32_u24_e32 v32, 0x88, v32
	v_and_b32_e32 v35, 12, v34
	s_lshl_b32 s5, s3, 4
	v_lshlrev_b32_e32 v29, 2, v29
	v_and_b32_e32 v30, 15, v1
	v_add_lshl_u32 v32, v32, v35, 1
	v_and_b32_e32 v35, 48, v28
	v_readlane_b32 s9, v255, 13
	s_add_i32 s2, 0, 0x16000
	v_or_b32_e32 v41, s5, v29
	v_readlane_b32 s8, v255, 16
	v_add_u32_e32 v37, s9, v35
	v_add_u32_e32 v38, s2, v33
	s_bfe_u32 s4, s24, 0x10006
	v_or_b32_e32 v39, s5, v30
	s_movk_i32 s10, 0x110
	v_lshl_add_u32 v42, v41, 1, s9
	s_lshl_b32 s2, s3, 8
	v_readlane_b32 s9, v255, 14
	v_add_u32_e32 v94, s8, v34
	s_movk_i32 s24, 0x90
	v_readlane_b32 s8, v253, 46
	v_mul_lo_u32 v40, v39, s10
	v_cmp_gt_u32_e64 s[40:41], 16, v28
	s_add_i32 s20, s9, s2
	v_ashrrev_i32_e32 v43, 3, v1
	v_and_b32_e32 v28, 7, v1
	s_add_i32 s21, 0, 0x20c00
	s_lshl_b32 s3, s3, 6
	v_mul_lo_u32 v39, v39, s24
	s_lshl_b32 s24, s4, 7
	s_add_i32 s5, s5, s8
	v_mul_lo_u32 v44, v43, s10
	v_lshlrev_b32_e32 v45, 5, v28
	v_lshl_add_u32 v92, v28, 6, s21
	v_cmp_eq_u32_e64 s[42:43], 0, v28
	v_and_b32_e32 v28, 0x7f, v1
	s_add_u32 s0, s0, s24
	v_add3_u32 v91, 0, v44, v45
	v_lshl_add_u32 v45, v28, 1, 0
	v_or_b32_e32 v96, s5, v29
	s_addc_u32 s1, s1, 0
	v_lshlrev_b32_e32 v28, 1, v30
	v_mov_b32_e32 v29, v3
	v_readlane_b32 s12, v255, 17
	v_lshl_add_u64 v[54:55], s[0:1], 0, v[28:29]
	s_lshl_b32 s0, s6, 5
	v_mul_lo_u32 v29, v31, s10
	s_add_i32 s1, s0, 0
	v_add3_u32 v99, 0, v29, v2
	v_add3_u32 v2, s12, v29, v2
	v_lshl_or_b32 v29, s4, 5, v30
	s_add_i32 s1, s1, 0xd800
	v_cmp_le_i32_e32 vcc, v41, v29
	v_and_b32_e32 v47, 48, v1
	v_add_u32_e32 v1, s12, v32
	v_add_u32_e32 v97, s1, v32
	v_add_u32_e32 v28, s0, v38
	v_cndmask_b32_e64 v32, 0, 1, vcc
	v_cmp_ge_i32_e32 vcc, v41, v29
	v_readlane_b32 s0, v253, 43
	v_add_u32_e32 v98, s21, v34
	v_cndmask_b32_e64 v34, 0, 1, vcc
	v_readlane_b32 s1, v253, 44
	v_cmp_lt_i32_e32 vcc, v41, v29
	v_add_u32_e32 v33, v38, v33
	v_cndmask_b32_e64 v32, v34, v32, s[0:1]
	v_and_b32_e32 v32, 1, v32
	v_cmp_eq_u32_e64 s[44:45], 1, v32
	v_or_b32_e32 v32, 1, v41
	v_cndmask_b32_e64 v34, 0, 1, vcc
	v_cmp_ge_i32_e32 vcc, v32, v29
	v_lshl_add_u32 v90, v31, 2, 0
	v_mul_u32_u24_e32 v31, 0x110, v29
	v_cndmask_b32_e64 v38, 0, 1, vcc
	v_cndmask_b32_e64 v34, v38, v34, s[0:1]
	v_and_b32_e32 v34, 1, v34
	v_cmp_eq_u32_e64 s[46:47], 1, v34
	v_or_b32_e32 v34, 2, v41
	v_cmp_le_i32_e32 vcc, v34, v29
	v_lshl_add_u32 v102, v29, 2, s20
	v_readlane_b32 s11, v255, 15
	v_cndmask_b32_e64 v38, 0, 1, vcc
	v_cmp_ge_i32_e32 vcc, v34, v29
	v_and_b32_e32 v44, 0xffffff0, v43
	v_lshl_or_b32 v46, s4, 6, v30
	v_cndmask_b32_e64 v56, 0, 1, vcc
	v_cndmask_b32_e64 v38, v56, v38, s[0:1]
	v_and_b32_e32 v38, 1, v38
	v_cmp_eq_u32_e64 s[48:49], 1, v38
	v_or_b32_e32 v38, 3, v41
	v_cmp_le_i32_e32 vcc, v38, v29
	v_add_u32_e32 v36, 0, v35
	s_mov_b32 s2, 0
	v_cndmask_b32_e64 v56, 0, 1, vcc
	v_cmp_ge_i32_e32 vcc, v38, v29
	v_lshl_add_u32 v93, v43, 2, s11
	v_add_u32_e32 v95, s24, v1
	v_cndmask_b32_e64 v57, 0, 1, vcc
	v_cndmask_b32_e64 v56, v57, v56, s[0:1]
	v_mul_u32_u24_e32 v57, 0x90, v29
	v_or_b32_e32 v29, 16, v29
	v_and_b32_e32 v56, 1, v56
	v_cmp_le_i32_e32 vcc, v41, v29
	v_cmp_eq_u32_e64 s[50:51], 1, v56
	v_add_u32_e32 v100, 0x2200, v99
	v_cndmask_b32_e64 v56, 0, 1, vcc
	v_cmp_ge_i32_e32 vcc, v41, v29
	v_add_u32_e32 v101, 0x2200, v2
	s_mov_b32 s4, 0x91b0
	v_cndmask_b32_e64 v58, 0, 1, vcc
	v_cndmask_b32_e64 v56, v58, v56, s[0:1]
	v_and_b32_e32 v56, 1, v56
	v_cmp_lt_i32_e32 vcc, v41, v29
	v_cmp_eq_u32_e64 s[52:53], 1, v56
	s_movk_i32 s5, 0xdc00
	v_cndmask_b32_e64 v56, 0, 1, vcc
	v_cmp_ge_i32_e32 vcc, v32, v29
	s_mov_b32 s6, 38
	v_add_u32_e32 v111, v37, v39
	v_cndmask_b32_e64 v32, 0, 1, vcc
	v_cndmask_b32_e64 v32, v32, v56, s[0:1]
	v_and_b32_e32 v32, 1, v32
	v_cmp_le_i32_e32 vcc, v34, v29
	v_cmp_eq_u32_e64 s[54:55], 1, v32
	v_mov_b32_e32 v56, 0
	v_cndmask_b32_e64 v32, 0, 1, vcc
	v_cmp_ge_i32_e32 vcc, v34, v29
	v_add_u32_e32 v113, v36, v40
	v_add_u32_e32 v114, v36, v31
	v_cndmask_b32_e64 v34, 0, 1, vcc
	v_cndmask_b32_e64 v32, v34, v32, s[0:1]
	v_and_b32_e32 v32, 1, v32
	v_cmp_le_i32_e32 vcc, v38, v29
	v_cmp_eq_u32_e64 s[56:57], 1, v32
	v_mul_u32_u24_e32 v34, 0x110, v46
	v_cndmask_b32_e64 v32, 0, 1, vcc
	v_cmp_ge_i32_e32 vcc, v38, v29
	v_lshlrev_b32_e32 v38, 2, v41
	v_add_u32_e32 v103, s11, v38
	v_cndmask_b32_e64 v29, 0, 1, vcc
	v_cndmask_b32_e64 v29, v29, v32, s[0:1]
	s_add_i32 s0, s3, 0
	v_and_b32_e32 v29, 1, v29
	v_or_b32_e32 v32, 15, v43
	v_add_u32_e32 v105, s0, v35
	s_addk_i32 s0, 0x4800
	v_cmp_eq_u32_e64 s[58:59], 1, v29
	v_mul_lo_u32 v29, v44, s10
	v_mul_lo_u32 v32, v32, s10
	v_add_u32_e32 v104, s9, v38
	v_mul_u32_u24_e32 v38, 0x110, v30
	v_add_u32_e32 v106, s0, v47
	s_add_i32 s0, s24, 0
	v_lshl_add_u32 v107, v30, 2, s0
	v_add_u32_e32 v108, v45, v29
	v_add_u32_e32 v109, v45, v32
	v_add_u32_e32 v110, v33, v34
	v_add_u32_e32 v112, v28, v38
	v_add_u32_e32 v115, v42, v57
	v_mov_b32_e32 v57, v56
	v_mov_b32_e32 v58, v56
	v_mov_b32_e32 v59, v56
	v_mov_b32_e32 v60, v56
	v_mov_b32_e32 v61, v56
	v_mov_b32_e32 v62, v56
	v_mov_b32_e32 v63, v56
	v_mov_b32_e32 v64, v56
	v_mov_b32_e32 v65, v56
	v_mov_b32_e32 v66, v56
	v_mov_b32_e32 v67, v56
	v_mov_b32_e32 v68, v56
	v_mov_b32_e32 v69, v56
	v_mov_b32_e32 v70, v56
	v_mov_b32_e32 v71, v56
	v_mov_b32_e32 v72, v56
	v_mov_b32_e32 v73, v56
	v_mov_b32_e32 v74, v56
	v_mov_b32_e32 v75, v56
	v_mov_b32_e32 v76, v56
	v_mov_b32_e32 v77, v56
	v_mov_b32_e32 v78, v56
	v_mov_b32_e32 v79, v56
	v_mov_b32_e32 v80, v56
	v_mov_b32_e32 v81, v56
	v_mov_b32_e32 v82, v56
	v_mov_b32_e32 v83, v56
	v_mov_b32_e32 v84, v56
	v_mov_b32_e32 v85, v56
	v_mov_b32_e32 v86, v56
	v_mov_b32_e32 v87, v56
	s_waitcnt vmcnt(0)
	s_branch .LBB0_6645

.LBB0_6645:
	v_add_u32_e32 v28, s5, v90
	v_add_u32_e32 v28, 0x2400, v28
	ds_read2_b32 v[32:33], v28 offset1:32
	s_waitcnt vmcnt(20)
	v_lshlrev_b32_e32 v28, 16, v8
	v_and_b32_e32 v29, 0xffff0000, v8
	v_lshlrev_b32_e32 v30, 16, v9
	v_and_b32_e32 v31, 0xffff0000, v9
	v_lshlrev_b32_e32 v34, 16, v10
	v_and_b32_e32 v35, 0xffff0000, v10
	v_lshlrev_b32_e32 v36, 16, v11
	v_and_b32_e32 v37, 0xffff0000, v11
	s_waitcnt lgkmcnt(0)
	v_mul_f32_e32 v28, v32, v28
	v_mul_f32_e32 v29, v32, v29
	v_mul_f32_e32 v30, v32, v30
	v_mul_f32_e32 v31, v32, v31
	ds_write_b128 v99, v[4:7] offset:37888
	s_waitcnt vmcnt(19)
	ds_write_b128 v100, v[12:15] offset:37888
	v_mul_f32_e32 v34, v32, v34
	v_mul_f32_e32 v35, v32, v35
	v_mul_f32_e32 v36, v32, v36
	v_mul_f32_e32 v32, v32, v37
	v_cvt_pk_bf16_f32 v28, v28, v29
	v_cvt_pk_bf16_f32 v29, v30, v31
	v_cvt_pk_bf16_f32 v30, v34, v35
	v_cvt_pk_bf16_f32 v31, v36, v32
	ds_write_b128 v99, v[28:31] offset:55296
	s_waitcnt vmcnt(17)
	v_lshlrev_b32_e32 v28, 16, v20
	v_and_b32_e32 v29, 0xffff0000, v20
	v_lshlrev_b32_e32 v30, 16, v21
	v_and_b32_e32 v31, 0xffff0000, v21
	v_lshlrev_b32_e32 v32, 16, v22
	v_and_b32_e32 v34, 0xffff0000, v22
	v_lshlrev_b32_e32 v35, 16, v23
	v_and_b32_e32 v36, 0xffff0000, v23
	v_mul_f32_e32 v28, v33, v28
	v_mul_f32_e32 v29, v33, v29
	v_mul_f32_e32 v30, v33, v30
	v_mul_f32_e32 v31, v33, v31
	s_add_i32 s20, s2, 1
	v_mul_f32_e32 v32, v33, v32
	v_mul_f32_e32 v34, v33, v34
	v_mul_f32_e32 v35, v33, v35
	v_mul_f32_e32 v33, v33, v36
	v_cvt_pk_bf16_f32 v28, v28, v29
	v_cvt_pk_bf16_f32 v29, v30, v31
	v_cvt_pk_bf16_f32 v30, v32, v34
	v_cvt_pk_bf16_f32 v31, v35, v33
	s_cmpk_eq_i32 s5, 0xff00
	ds_write_b128 v100, v[28:31] offset:55296
	ds_write_b128 v2, v[16:19]
	s_waitcnt vmcnt(16)
	ds_write_b128 v101, v[24:27]
	s_waitcnt lgkmcnt(0)
	s_barrier
	s_cbranch_scc1 .LBB0_6650
	v_readlane_b32 s0, v253, 41
	v_readlane_b32 s1, v253, 42
	s_andn2_b64 vcc, exec, s[0:1]
	s_mov_b32 s0, s20
	s_cbranch_vccnz .LBB0_6649
	s_cmp_gt_u32 s2, 2
	s_mov_b32 s0, s6
	s_cbranch_scc1 .LBB0_6649
	s_sub_i32 s0, 2, s2

.LBB0_6656:
	s_or_b64 exec, exec, s[0:1]
	ds_read_u16 v28, v108 offset:55296
	s_waitcnt lgkmcnt(1)
	ds_read_u16 v29, v108 offset:55568
	ds_read_u16 v30, v108 offset:55840
	ds_read_u16 v31, v108 offset:56112
	ds_read_u16 v32, v108 offset:56384
	ds_read_u16 v33, v108 offset:56656
	ds_read_u16 v34, v108 offset:56928
	ds_read_u16 v35, v108 offset:57200
	s_waitcnt lgkmcnt(7)
	v_lshlrev_b32_e32 v28, 16, v28
	v_add_f32_e32 v28, 0, v28
	s_waitcnt lgkmcnt(6)
	v_lshlrev_b32_e32 v29, 16, v29
	v_add_f32_e32 v28, v28, v29
	s_waitcnt lgkmcnt(5)
	v_lshlrev_b32_e32 v29, 16, v30
	v_add_f32_e32 v28, v28, v29
	s_waitcnt lgkmcnt(4)
	v_lshlrev_b32_e32 v29, 16, v31
	v_add_f32_e32 v28, v28, v29
	s_waitcnt lgkmcnt(3)
	v_lshlrev_b32_e32 v29, 16, v32
	v_add_f32_e32 v28, v28, v29
	s_waitcnt lgkmcnt(2)
	v_lshlrev_b32_e32 v29, 16, v33
	v_add_f32_e32 v28, v28, v29
	s_waitcnt lgkmcnt(1)
	v_lshlrev_b32_e32 v29, 16, v34
	v_add_f32_e32 v28, v28, v29
	s_waitcnt lgkmcnt(0)
	v_lshlrev_b32_e32 v29, 16, v35
	v_add_f32_e32 v28, v28, v29
	ds_read_u16 v29, v108 offset:57472
	ds_read_u16 v30, v108 offset:57744
	ds_read_u16 v31, v108 offset:58016
	ds_read_u16 v32, v108 offset:58288
	ds_read_u16 v33, v108 offset:58560
	ds_read_u16 v34, v108 offset:58832
	ds_read_u16 v35, v108 offset:59104
	ds_read_u16 v36, v109 offset:55296
	s_waitcnt lgkmcnt(7)
	v_lshlrev_b32_e32 v29, 16, v29
	v_add_f32_e32 v28, v28, v29
	s_waitcnt lgkmcnt(6)
	v_lshlrev_b32_e32 v29, 16, v30
	v_add_f32_e32 v28, v28, v29
	s_waitcnt lgkmcnt(5)
	v_lshlrev_b32_e32 v29, 16, v31
	v_add_f32_e32 v28, v28, v29
	s_waitcnt lgkmcnt(4)
	v_lshlrev_b32_e32 v29, 16, v32
	v_add_f32_e32 v28, v28, v29
	s_waitcnt lgkmcnt(3)
	v_lshlrev_b32_e32 v29, 16, v33
	v_add_f32_e32 v28, v28, v29
	s_waitcnt lgkmcnt(2)
	v_lshlrev_b32_e32 v29, 16, v34
	v_add_f32_e32 v28, v28, v29
	s_waitcnt lgkmcnt(1)
	v_lshlrev_b32_e32 v29, 16, v35
	v_add_f32_e32 v28, v28, v29
	s_waitcnt lgkmcnt(0)
	v_lshlrev_b32_e32 v29, 16, v36
	v_add_f32_e32 v28, v28, v29
	ds_write_b32 v94, v28
	s_waitcnt lgkmcnt(0)
	s_barrier
	ds_read_b128 v[28:31], v113 offset:37888
	ds_read_b128 v[32:35], v113 offset:37952
	ds_read_b128 v[36:39], v110
	ds_read_b128 v[40:43], v110 offset:64
	s_waitcnt lgkmcnt(1)
	v_mfma_f32_16x16x32_bf16 v[36:39], v[28:31], v[36:39], 0
	ds_read_b128 v[44:47], v113 offset:38016
	ds_read_b128 v[116:119], v113 offset:38080
	s_cmp_gt_u32 s2, 3
	s_cselect_b32 s0, 39, 3
	s_waitcnt lgkmcnt(2)
	v_mfma_f32_16x16x32_bf16 v[36:39], v[32:35], v[40:43], v[36:39]
	ds_read_b128 v[40:43], v110 offset:128
	ds_read_b128 v[120:123], v110 offset:192
	s_add_i32 s0, s0, s6
	s_sub_i32 s3, s0, 38
	s_waitcnt lgkmcnt(1)
	v_mfma_f32_16x16x32_bf16 v[36:39], v[44:47], v[40:43], v[36:39]
	v_readlane_b32 s0, v253, 43
	v_readlane_b32 s1, v253, 44
	s_and_b64 s[0:1], s[0:1], exec
	s_waitcnt lgkmcnt(0)
	v_mfma_f32_16x16x32_bf16 v[40:43], v[116:119], v[120:123], v[36:39]
	s_nop 2
	ds_read_b128 v[36:39], v110 offset:4352
	ds_read_b128 v[120:123], v110 offset:4416
	s_cselect_b32 s0, s2, s3
	s_add_i32 s1, s4, 0
	s_waitcnt lgkmcnt(1)
	v_mfma_f32_16x16x32_bf16 v[36:39], v[28:31], v[36:39], 0
	s_waitcnt lgkmcnt(0)
	v_mfma_f32_16x16x32_bf16 v[36:39], v[32:35], v[120:123], v[36:39]
	ds_read_b128 v[120:123], v110 offset:4480
	ds_read_b128 v[124:127], v110 offset:4544
	s_waitcnt lgkmcnt(1)
	v_mfma_f32_16x16x32_bf16 v[36:39], v[44:47], v[120:123], v[36:39]
	s_waitcnt lgkmcnt(0)
	v_mfma_f32_16x16x32_bf16 v[120:123], v[116:119], v[124:127], v[36:39]
	s_nop 5
	ds_read_b128 v[36:39], v110 offset:8704
	ds_read_b128 v[124:127], v110 offset:8768
	s_waitcnt lgkmcnt(1)
	v_mfma_f32_16x16x32_bf16 v[36:39], v[28:31], v[36:39], 0
	s_waitcnt lgkmcnt(0)
	v_mfma_f32_16x16x32_bf16 v[36:39], v[32:35], v[124:127], v[36:39]
	ds_read_b128 v[124:127], v110 offset:8832
	ds_read_b128 v[128:131], v110 offset:8896
	s_waitcnt lgkmcnt(1)
	v_mfma_f32_16x16x32_bf16 v[36:39], v[44:47], v[124:127], v[36:39]
	ds_read_b128 v[124:127], v110 offset:13056
	s_waitcnt lgkmcnt(1)
	v_mfma_f32_16x16x32_bf16 v[128:131], v[116:119], v[128:131], v[36:39]
	s_nop 4
	ds_read_b128 v[36:39], v110 offset:13120
	s_waitcnt lgkmcnt(1)
	v_mfma_f32_16x16x32_bf16 v[28:31], v[28:31], v[124:127], 0
	ds_read_b128 v[124:127], v110 offset:13184
	s_waitcnt lgkmcnt(1)
	v_mfma_f32_16x16x32_bf16 v[28:31], v[32:35], v[36:39], v[28:31]
	ds_read_b128 v[32:35], v110 offset:13248
	v_mov_b32_e32 v36, s1
	ds_read2_b32 v[88:89], v36 offset1:36
	s_waitcnt lgkmcnt(2)
	v_mfma_f32_16x16x32_bf16 v[28:31], v[44:47], v[124:127], v[28:31]
	s_waitcnt lgkmcnt(1)
	v_mfma_f32_16x16x32_bf16 v[44:47], v[116:119], v[32:35], v[28:31]
	s_nop 5
	v_add_u32_e32 v28, s5, v106
	ds_read_b128 v[36:39], v28 offset:9216
	ds_read_b128 v[116:119], v111
	ds_read_b128 v[124:127], v111 offset:64
	ds_read_b64_tr_b16 v[28:29], v95 offset:0
	ds_read_b64_tr_b16 v[30:31], v95 offset:0x440
	ds_read_b64_tr_b16 v[32:33], v95 offset:0x2200
	ds_read_b64_tr_b16 v[34:35], v95 offset:0x2640
	ds_read_b64_tr_b16 v[132:133], v95 offset:32
	ds_read_b64_tr_b16 v[134:135], v95 offset:0x460
	ds_read_b64_tr_b16 v[136:137], v95 offset:0x2220
	ds_read_b64_tr_b16 v[138:139], v95 offset:0x2660
	ds_read_b64_tr_b16 v[140:141], v95 offset:64
	ds_read_b64_tr_b16 v[142:143], v95 offset:0x480
	ds_read_b64_tr_b16 v[144:145], v95 offset:0x2240
	ds_read_b64_tr_b16 v[146:147], v95 offset:0x2680
	ds_read_b64_tr_b16 v[148:149], v95 offset:0x60
	ds_read_b64_tr_b16 v[150:151], v95 offset:0x4a0
	ds_read_b64_tr_b16 v[152:153], v95 offset:0x2260
	ds_read_b64_tr_b16 v[154:155], v95 offset:0x26a0
	s_waitcnt lgkmcnt(0)
	s_waitcnt lgkmcnt(2)
	v_pk_mul_f32 v[42:43], v[42:43], v[38:39]
	v_pk_mul_f32 v[40:41], v[40:41], v[36:37]
	v_pk_mul_f32 v[46:47], v[46:47], v[38:39]
	v_pk_mul_f32 v[44:45], v[44:45], v[36:37]
	s_waitcnt lgkmcnt(1)
	v_mfma_f32_16x16x32_bf16 v[28:31], v[116:119], v[28:31], v[40:43]
	s_cmp_gt_i32 s0, 3
	s_cselect_b64 s[2:3], -1, 0
	s_or_b64 s[2:3], s[36:37], s[2:3]
	s_waitcnt lgkmcnt(0)
	v_mfma_f32_16x16x32_bf16 v[28:31], v[124:127], v[32:35], v[28:31]
	v_mul_f32_e64 v34, v122, v38
	v_mul_f32_e64 v35, v123, v39
	v_pk_mul_f32 v[32:33], v[120:121], v[36:37]
	v_pk_mul_f32 v[42:43], v[130:131], v[38:39]
	v_pk_mul_f32 v[40:41], v[128:129], v[36:37]
	v_mfma_f32_16x16x32_bf16 v[32:35], v[116:119], v[132:135], v[32:35]
	s_andn2_b64 vcc, exec, s[2:3]
	v_mfma_f32_16x16x32_bf16 v[40:43], v[116:119], v[140:143], v[40:43]
	v_mfma_f32_16x16x32_bf16 v[44:47], v[116:119], v[148:151], v[44:47]
	v_mfma_f32_16x16x32_bf16 v[32:35], v[124:127], v[136:139], v[32:35]
	v_mfma_f32_16x16x32_bf16 v[40:43], v[124:127], v[144:147], v[40:43]
	v_mfma_f32_16x16x32_bf16 v[44:47], v[124:127], v[152:155], v[44:47]
	s_cbranch_vccnz .Lml_nostore
	ds_read_b128 v[116:119], v103
	ds_read_b128 v[120:123], v104
	ds_read_b128 v[124:127], v104 offset:256
	ds_read_b128 v[128:131], v104 offset:512
	ds_read_b128 v[132:135], v104 offset:768
	s_waitcnt lgkmcnt(2)
	v_add_f32_e32 v123, v123, v127
	s_waitcnt lgkmcnt(0)
	v_add_f32_e32 v127, v131, v135
	v_add_f32_e32 v123, v123, v127
	v_fmac_f32_e32 v123, v39, v119
	v_add_u32_e32 v39, s5, v105
	ds_read_b128 v[136:139], v39 offset:36864
	s_waitcnt lgkmcnt(0)
	v_max_f32_e32 v39, v139, v139
	v_max_f32_e64 v39, |v123|, v39
	v_div_scale_f32 v119, s[2:3], v39, v39, 1.0
	v_rcp_f32_e32 v123, v119
	s_nop 0
	v_fma_f32 v127, -v119, v123, 1.0
	v_fmac_f32_e32 v123, v127, v123
	v_div_scale_f32 v127, vcc, 1.0, v39, 1.0
	v_mul_f32_e32 v131, v127, v123
	v_fma_f32 v135, -v119, v131, v127
	v_fmac_f32_e32 v131, v135, v123
	v_fma_f32 v119, -v119, v131, v127
	v_div_fmas_f32 v119, v119, v123, v131
	v_div_fixup_f32 v39, v119, v39, 1.0
	v_add_f32_e32 v119, v122, v126
	v_add_f32_e32 v122, v130, v134
	v_add_f32_e32 v119, v119, v122
	v_fmac_f32_e32 v119, v38, v118
	v_max_f32_e32 v38, v138, v138
	v_max_f32_e64 v38, |v119|, v38
	v_div_scale_f32 v118, s[2:3], v38, v38, 1.0
	v_rcp_f32_e32 v119, v118
	s_nop 0
	v_fma_f32 v122, -v118, v119, 1.0
	v_fmac_f32_e32 v119, v122, v119
	v_div_scale_f32 v122, vcc, 1.0, v38, 1.0
	v_mul_f32_e32 v123, v122, v119
	v_fma_f32 v126, -v118, v123, v122
	v_fmac_f32_e32 v123, v126, v119
	v_fma_f32 v118, -v118, v123, v122
	v_div_fmas_f32 v118, v118, v119, v123
	v_div_fixup_f32 v38, v118, v38, 1.0
	v_add_f32_e32 v118, v121, v125
	v_add_f32_e32 v119, v129, v133
	v_add_f32_e32 v118, v118, v119
	v_fmac_f32_e32 v118, v37, v117
	v_max_f32_e32 v37, v137, v137
	v_max_f32_e64 v37, |v118|, v37
	v_div_scale_f32 v117, s[2:3], v37, v37, 1.0
	v_rcp_f32_e32 v118, v117
	s_nop 0
	v_fma_f32 v119, -v117, v118, 1.0
	v_fmac_f32_e32 v118, v119, v118
	v_div_scale_f32 v119, vcc, 1.0, v37, 1.0
	v_mul_f32_e32 v121, v119, v118
	v_fma_f32 v122, -v117, v121, v119
	v_fmac_f32_e32 v121, v122, v118
	v_fma_f32 v117, -v117, v121, v119
	v_div_fmas_f32 v117, v117, v118, v121
	v_div_fixup_f32 v117, v117, v37, 1.0
	v_add_f32_e32 v37, v120, v124
	v_add_f32_e32 v118, v128, v132
	v_add_f32_e32 v37, v37, v118
	v_fmac_f32_e32 v37, v36, v116
	v_max_f32_e32 v36, v136, v136
	v_max_f32_e64 v36, |v37|, v36
	v_div_scale_f32 v37, s[2:3], v36, v36, 1.0
	v_rcp_f32_e32 v116, v37
	s_nop 0
	v_fma_f32 v118, -v37, v116, 1.0
	v_fmac_f32_e32 v116, v118, v116
	v_div_scale_f32 v118, vcc, 1.0, v36, 1.0
	v_mul_f32_e32 v119, v118, v116
	v_fma_f32 v120, -v37, v119, v118
	v_fmac_f32_e32 v119, v120, v116
	v_fma_f32 v37, -v37, v119, v118
	v_div_fmas_f32 v37, v37, v116, v119
	v_div_fixup_f32 v116, v37, v36, 1.0
	v_lshl_add_u32 v36, s0, 6, v96
	v_ashrrev_i32_e32 v37, 31, v36
	v_lshlrev_b64 v[36:37], 10, v[36:37]
	v_mul_f32_e32 v28, v28, v116
	v_lshl_add_u64 v[36:37], v[54:55], 0, v[36:37]
	v_cvt_pk_bf16_f32 v28, v28, v28
	global_store_short v[36:37], v28, off
	v_mul_f32_e32 v28, v29, v117
	v_cvt_pk_bf16_f32 v28, v28, v28
	global_store_short v[36:37], v28, off offset:1024
	v_mul_f32_e32 v28, v30, v38
	v_cvt_pk_bf16_f32 v28, v28, v28
	global_store_short v[36:37], v28, off offset:2048
	v_mul_f32_e32 v28, v31, v39
	v_cvt_pk_bf16_f32 v28, v28, v28
	global_store_short v[36:37], v28, off offset:3072
	v_mul_f32_e32 v28, v32, v116
	v_cvt_pk_bf16_f32 v28, v28, v28
	global_store_short v[36:37], v28, off offset:32
	v_mul_f32_e32 v28, v33, v117
	v_cvt_pk_bf16_f32 v28, v28, v28
	global_store_short v[36:37], v28, off offset:1056
	v_mul_f32_e32 v28, v34, v38
	v_cvt_pk_bf16_f32 v28, v28, v28
	global_store_short v[36:37], v28, off offset:2080
	v_mul_f32_e32 v28, v35, v39
	v_cvt_pk_bf16_f32 v28, v28, v28
	global_store_short v[36:37], v28, off offset:3104
	v_mul_f32_e32 v28, v40, v116
	v_cvt_pk_bf16_f32 v28, v28, v28
	global_store_short v[36:37], v28, off offset:64
	v_mul_f32_e32 v28, v41, v117
	v_cvt_pk_bf16_f32 v28, v28, v28
	global_store_short v[36:37], v28, off offset:1088
	v_mul_f32_e32 v28, v42, v38
	v_cvt_pk_bf16_f32 v28, v28, v28
	global_store_short v[36:37], v28, off offset:2112
	v_mul_f32_e32 v28, v43, v39
	v_cvt_pk_bf16_f32 v28, v28, v28
	global_store_short v[36:37], v28, off offset:3136
	v_mul_f32_e32 v28, v44, v116
	v_cvt_pk_bf16_f32 v28, v28, v28
	global_store_short v[36:37], v28, off offset:96
	v_mul_f32_e32 v28, v45, v117
	v_cvt_pk_bf16_f32 v28, v28, v28
	global_store_short v[36:37], v28, off offset:1120
	v_mul_f32_e32 v28, v46, v38
	v_cvt_pk_bf16_f32 v28, v28, v28
	global_store_short v[36:37], v28, off offset:2144
	v_mul_f32_e32 v28, v47, v39
	v_cvt_pk_bf16_f32 v28, v28, v28
	global_store_short v[36:37], v28, off offset:3168
	s_branch .LBB0_6658
.Lml_nostore:
	s_waitcnt vmcnt(0)
.LBB0_6658:
	ds_read_b64_tr_b16 v[28:29], v97 offset:0
	ds_read_b64_tr_b16 v[30:31], v97 offset:0x440
	ds_read_b64_tr_b16 v[32:33], v97 offset:0x2200
	ds_read_b64_tr_b16 v[34:35], v97 offset:0x2640
	ds_read_b64_tr_b16 v[36:37], v1 offset:0
	ds_read_b64_tr_b16 v[38:39], v1 offset:0x440
	ds_read_b64_tr_b16 v[40:41], v1 offset:0x2200
	ds_read_b64_tr_b16 v[42:43], v1 offset:0x2640
	ds_read_b64_tr_b16 v[44:45], v1 offset:32
	ds_read_b64_tr_b16 v[46:47], v1 offset:0x460
	ds_read_b64_tr_b16 v[116:117], v1 offset:0x2220
	ds_read_b64_tr_b16 v[118:119], v1 offset:0x2660
	ds_read_b64_tr_b16 v[120:121], v1 offset:64
	ds_read_b64_tr_b16 v[122:123], v1 offset:0x480
	ds_read_b64_tr_b16 v[124:125], v1 offset:0x2240
	ds_read_b64_tr_b16 v[126:127], v1 offset:0x2680
	ds_read_b64_tr_b16 v[128:129], v1 offset:0x60
	ds_read_b64_tr_b16 v[130:131], v1 offset:0x4a0
	ds_read_b64_tr_b16 v[132:133], v1 offset:0x2260
	ds_read_b64_tr_b16 v[134:135], v1 offset:0x26a0
	ds_read_b64_tr_b16 v[136:137], v1 offset:0x80
	ds_read_b64_tr_b16 v[138:139], v1 offset:0x4c0
	ds_read_b64_tr_b16 v[140:141], v1 offset:0x2280
	ds_read_b64_tr_b16 v[142:143], v1 offset:0x26c0
	ds_read_b64_tr_b16 v[144:145], v1 offset:0xa0
	ds_read_b64_tr_b16 v[146:147], v1 offset:0x4e0
	ds_read_b64_tr_b16 v[148:149], v1 offset:0x22a0
	ds_read_b64_tr_b16 v[150:151], v1 offset:0x26e0
	ds_read_b64_tr_b16 v[152:153], v1 offset:0xc0
	ds_read_b64_tr_b16 v[154:155], v1 offset:0x500
	ds_read_b64_tr_b16 v[156:157], v1 offset:0x22c0
	ds_read_b64_tr_b16 v[158:159], v1 offset:0x2700
	ds_read_b64_tr_b16 v[160:161], v1 offset:0xe0
	ds_read_b64_tr_b16 v[162:163], v1 offset:0x520
	ds_read_b64_tr_b16 v[164:165], v1 offset:0x22e0
	ds_read_b64_tr_b16 v[166:167], v1 offset:0x2720
	s_waitcnt lgkmcnt(0)
	s_nop 0
	v_mfma_f32_16x16x32_bf16 v[36:39], v[28:31], v[36:39], 0
	s_barrier
	s_nop 2
	v_mfma_f32_16x16x32_bf16 v[36:39], v[32:35], v[40:43], v[36:39]
	v_mfma_f32_16x16x32_bf16 v[40:43], v[28:31], v[44:47], 0
	v_mfma_f32_16x16x32_bf16 v[40:43], v[32:35], v[116:119], v[40:43]
	v_mfma_f32_16x16x32_bf16 v[44:47], v[28:31], v[120:123], 0
	v_mov_b32_e32 v120, v89
	s_nop 3
	v_pk_mul_f32 v[38:39], v[120:121], v[38:39] op_sel_hi:[0,1]
	v_pk_mul_f32 v[36:37], v[120:121], v[36:37] op_sel_hi:[0,1]
	v_mfma_f32_16x16x32_bf16 v[116:119], v[28:31], v[128:131], 0
	v_mul_f32_e64 v42, v120, v42
	v_mul_f32_e64 v43, v120, v43
	v_pk_fma_f32 v[58:59], v[58:59], v[88:89], v[38:39] op_sel_hi:[1,0,1]
	v_pk_fma_f32 v[56:57], v[56:57], v[88:89], v[36:37] op_sel_hi:[1,0,1]
	v_mfma_f32_16x16x32_bf16 v[44:47], v[32:35], v[124:127], v[44:47]
	v_fma_f32 v62, v62, v88, v42
	v_fma_f32 v63, v63, v88, v43
	v_mfma_f32_16x16x32_bf16 v[36:39], v[32:35], v[132:135], v[116:119]
	s_nop 2
	v_mul_f32_e64 v116, v120, v40
	v_mul_f32_e64 v117, v120, v41
	v_mfma_f32_16x16x32_bf16 v[40:43], v[28:31], v[136:139], 0
	v_mul_f32_e64 v46, v120, v46
	v_mul_f32_e64 v47, v120, v47
	v_pk_mul_f32 v[44:45], v[120:121], v[44:45] op_sel_hi:[0,1]
	v_pk_fma_f32 v[66:67], v[66:67], v[88:89], v[46:47] op_sel_hi:[1,0,1]
	v_mfma_f32_16x16x32_bf16 v[40:43], v[32:35], v[140:143], v[40:43]
	v_fma_f32 v64, v64, v88, v44
	v_fma_f32 v65, v65, v88, v45
	v_pk_mul_f32 v[38:39], v[120:121], v[38:39] op_sel_hi:[0,1]
	v_pk_mul_f32 v[36:37], v[120:121], v[36:37] op_sel_hi:[0,1]
	v_mfma_f32_16x16x32_bf16 v[44:47], v[28:31], v[144:147], 0
	v_fma_f32 v70, v70, v88, v38
	v_fma_f32 v71, v71, v88, v39
	s_nop 0
	v_pk_mul_f32 v[42:43], v[120:121], v[42:43] op_sel_hi:[0,1]
	v_pk_fma_f32 v[68:69], v[68:69], v[88:89], v[36:37] op_sel_hi:[1,0,1]
	v_mfma_f32_16x16x32_bf16 v[36:39], v[32:35], v[148:151], v[44:47]
	v_fma_f32 v74, v74, v88, v42
	v_fma_f32 v75, v75, v88, v43
	v_pk_fma_f32 v[60:61], v[60:61], v[88:89], v[116:117] op_sel_hi:[1,0,1]
	v_pk_mul_f32 v[44:45], v[120:121], v[40:41] op_sel_hi:[0,1]
	v_mfma_f32_16x16x32_bf16 v[40:43], v[28:31], v[152:155], 0
	v_fma_f32 v72, v72, v88, v44
	v_fma_f32 v73, v73, v88, v45
	s_nop 0
	v_pk_mul_f32 v[44:45], v[120:121], v[38:39] op_sel_hi:[0,1]
	v_pk_mul_f32 v[46:47], v[120:121], v[36:37] op_sel_hi:[0,1]
	v_mfma_f32_16x16x32_bf16 v[28:31], v[28:31], v[160:163], 0
	v_fma_f32 v78, v78, v88, v44
	v_fma_f32 v79, v79, v88, v45
	v_pk_fma_f32 v[76:77], v[76:77], v[88:89], v[46:47] op_sel_hi:[1,0,1]
	v_mfma_f32_16x16x32_bf16 v[28:31], v[32:35], v[164:167], v[28:31]
	v_mfma_f32_16x16x32_bf16 v[36:39], v[32:35], v[156:159], v[40:43]
	s_nop 6
	v_mul_f32_e64 v28, v120, v28
	v_mul_f32_e64 v29, v120, v29
	v_pk_fma_f32 v[84:85], v[84:85], v[88:89], v[28:29] op_sel_hi:[1,0,1]
	v_cvt_pk_bf16_f32 v28, v56, v57
	v_cvt_pk_bf16_f32 v29, v58, v59
	ds_write_b64 v112, v[28:29]
	v_cvt_pk_bf16_f32 v28, v60, v61
	v_cvt_pk_bf16_f32 v29, v62, v63
	ds_write_b64 v112, v[28:29] offset:4352
	v_cvt_pk_bf16_f32 v28, v64, v65
	v_cvt_pk_bf16_f32 v29, v66, v67
	ds_write_b64 v112, v[28:29] offset:8704
	v_cvt_pk_bf16_f32 v28, v68, v69
	v_cvt_pk_bf16_f32 v29, v70, v71
	ds_write_b64 v112, v[28:29] offset:13056
	v_cvt_pk_bf16_f32 v28, v72, v73
	v_cvt_pk_bf16_f32 v29, v74, v75
	v_pk_mul_f32 v[38:39], v[120:121], v[38:39] op_sel_hi:[0,1]
	v_pk_mul_f32 v[36:37], v[120:121], v[36:37] op_sel_hi:[0,1]
	v_pk_mul_f32 v[30:31], v[120:121], v[30:31] op_sel_hi:[0,1]
	ds_write_b64 v112, v[28:29] offset:17408
	v_cvt_pk_bf16_f32 v28, v76, v77
	v_cvt_pk_bf16_f32 v29, v78, v79
	v_pk_fma_f32 v[82:83], v[82:83], v[88:89], v[38:39] op_sel_hi:[1,0,1]
	v_pk_fma_f32 v[80:81], v[80:81], v[88:89], v[36:37] op_sel_hi:[1,0,1]
	v_pk_fma_f32 v[86:87], v[86:87], v[88:89], v[30:31] op_sel_hi:[1,0,1]
	ds_write_b64 v112, v[28:29] offset:21760
	v_cvt_pk_bf16_f32 v28, v80, v81
	v_cvt_pk_bf16_f32 v29, v82, v83
	ds_write_b64 v112, v[28:29] offset:26112
	v_cvt_pk_bf16_f32 v28, v84, v85
	v_cvt_pk_bf16_f32 v29, v86, v87
	ds_write_b64 v112, v[28:29] offset:30464
	s_and_saveexec_b64 s[0:1], s[38:39]
	s_cbranch_execz .LBB0_6644
	ds_read2st64_b32 v[28:29], v94 offset1:2
	ds_read2st64_b32 v[30:31], v94 offset0:4 offset1:6
	ds_read_b32 v32, v98
	s_waitcnt lgkmcnt(2)
	v_mov_b32_e32 v34, v28
	s_waitcnt lgkmcnt(1)
	v_mov_b32_e32 v35, v30
	v_mov_b32_e32 v30, v29
	v_pk_add_f32 v[28:29], v[34:35], v[30:31]
	s_nop 0
	v_pk_add_f32 v[28:29], v[28:29], v[28:29] op_sel_hi:[0,1]
	v_mov_b32_e32 v33, v29
	s_waitcnt lgkmcnt(0)
	v_pk_mul_f32 v[28:29], v[88:89], v[32:33]
	s_nop 0
	v_add_f32_e32 v28, v28, v29
	ds_write_b32 v98, v28
	s_branch .LBB0_6644

.LBB0_7153:
	s_and_b64 s[2:3], s[50:51], exec
	s_cselect_b32 s2, 8, s4
	v_lshl_or_b32 v134, s48, 8, v162
	v_lshlrev_b64 v[132:133], 13, v[132:133]
	s_mul_hi_i32 s3, s2, 0xc000
	s_mul_i32 s2, s2, 0xc000
	v_ashrrev_i32_e32 v135, 31, v134
	v_lshl_add_u64 v[132:133], s[52:53], 0, v[132:133]
	s_add_u32 s2, s62, s2
	v_lshlrev_b64 v[168:169], 2, v[134:135]
	s_addc_u32 s3, s63, s3
	v_lshl_add_u64 v[158:159], v[132:133], 0, v[168:169]
	v_lshl_add_u64 v[134:135], s[2:3], 0, v[168:169]
	v_readlane_b32 s4, v253, 51
	v_readlane_b32 s5, v253, 52
	v_lshlrev_b64 v[132:133], 13, v[160:161]
	s_mov_b32 s3, 0
	v_lshl_add_u64 v[132:133], s[4:5], 0, v[132:133]
	v_lshl_add_u64 v[156:157], v[132:133], 0, v[168:169]
	global_load_dwordx4 v[168:171], v[134:135], off
	global_load_dwordx4 v[172:175], v[134:135], off offset:64
	global_load_dwordx4 v[176:179], v[134:135], off offset:512
	global_load_dwordx4 v[180:183], v[134:135], off offset:576
	global_load_dwordx4 v[204:207], v[158:159], off
	global_load_dwordx4 v[208:211], v[158:159], off offset:64
	global_load_dwordx4 v[212:215], v[158:159], off offset:512
	global_load_dwordx4 v[216:219], v[158:159], off offset:576
	s_mov_b32 s2, 0x20000
	v_lshl_add_u64 v[164:165], v[158:159], 0, s[2:3]
	global_load_dwordx4 v[226:229], v[164:165], off
	global_load_dwordx4 v[230:233], v[164:165], off offset:64
	global_load_dwordx4 v[234:237], v[164:165], off offset:512
	global_load_dwordx4 v[238:241], v[164:165], off offset:576
	s_mov_b32 s2, 0x40000
	v_lshl_add_u64 v[164:165], v[158:159], 0, s[2:3]
	global_load_dwordx4 v[186:189], v[164:165], off
	global_load_dwordx4 v[194:197], v[164:165], off offset:64
	global_load_dwordx4 v[198:201], v[164:165], off offset:512
	global_load_dwordx4 v[242:245], v[164:165], off offset:576
	s_waitcnt vmcnt(8)
	v_pk_fma_f32 v[206:207], v[130:131], v[170:171], v[206:207]
	v_pk_fma_f32 v[204:205], v[128:129], v[168:169], v[204:205]
	v_pk_fma_f32 v[210:211], v[126:127], v[174:175], v[210:211]
	v_pk_fma_f32 v[208:209], v[124:125], v[172:173], v[208:209]
	v_pk_fma_f32 v[214:215], v[122:123], v[178:179], v[214:215]
	v_pk_fma_f32 v[212:213], v[120:121], v[176:177], v[212:213]
	v_pk_fma_f32 v[218:219], v[114:115], v[182:183], v[218:219]
	v_pk_fma_f32 v[216:217], v[112:113], v[180:181], v[216:217]
	global_store_dwordx4 v[156:157], v[204:207], off
	global_store_dwordx4 v[156:157], v[208:211], off offset:64
	global_store_dwordx4 v[156:157], v[212:215], off offset:512
	global_store_dwordx4 v[156:157], v[216:219], off offset:576
	s_mov_b32 s2, 0x60000
	v_lshl_add_u64 v[164:165], v[158:159], 0, s[2:3]
	global_load_dwordx4 v[204:207], v[164:165], off
	global_load_dwordx4 v[208:211], v[164:165], off offset:64
	global_load_dwordx4 v[212:215], v[164:165], off offset:512
	global_load_dwordx4 v[216:219], v[164:165], off offset:576
	s_waitcnt vmcnt(12)
	v_pk_fma_f32 v[228:229], v[118:119], v[170:171], v[228:229]
	v_pk_fma_f32 v[226:227], v[116:117], v[168:169], v[226:227]
	v_pk_fma_f32 v[232:233], v[110:111], v[174:175], v[232:233]
	v_pk_fma_f32 v[230:231], v[108:109], v[172:173], v[230:231]
	v_pk_fma_f32 v[236:237], v[106:107], v[178:179], v[236:237]
	v_pk_fma_f32 v[234:235], v[104:105], v[176:177], v[234:235]
	v_pk_fma_f32 v[240:241], v[98:99], v[182:183], v[240:241]
	v_pk_fma_f32 v[238:239], v[96:97], v[180:181], v[238:239]
	s_mov_b32 s2, 0x20000
	v_lshl_add_u64 v[136:137], v[156:157], 0, s[2:3]
	global_store_dwordx4 v[136:137], v[226:229], off
	global_store_dwordx4 v[136:137], v[230:233], off offset:64
	global_store_dwordx4 v[136:137], v[234:237], off offset:512
	global_store_dwordx4 v[136:137], v[238:241], off offset:576
	s_mov_b32 s2, 0x100000
	v_lshl_add_u64 v[164:165], v[158:159], 0, s[2:3]
	global_load_dwordx4 v[226:229], v[164:165], off
	global_load_dwordx4 v[230:233], v[164:165], off offset:64
	global_load_dwordx4 v[234:237], v[164:165], off offset:512
	global_load_dwordx4 v[238:241], v[164:165], off offset:576
	s_waitcnt vmcnt(16)
	v_pk_fma_f32 v[188:189], v[102:103], v[170:171], v[188:189]
	v_pk_fma_f32 v[186:187], v[100:101], v[168:169], v[186:187]
	v_pk_fma_f32 v[196:197], v[94:95], v[174:175], v[196:197]
	v_pk_fma_f32 v[194:195], v[92:93], v[172:173], v[194:195]
	v_pk_fma_f32 v[200:201], v[90:91], v[178:179], v[200:201]
	v_pk_fma_f32 v[198:199], v[88:89], v[176:177], v[198:199]
	v_pk_fma_f32 v[244:245], v[82:83], v[182:183], v[244:245]
	v_pk_fma_f32 v[242:243], v[80:81], v[180:181], v[242:243]
	s_mov_b32 s2, 0x40000
	v_lshl_add_u64 v[136:137], v[156:157], 0, s[2:3]
	global_store_dwordx4 v[136:137], v[186:189], off
	global_store_dwordx4 v[136:137], v[194:197], off offset:64
	global_store_dwordx4 v[136:137], v[198:201], off offset:512
	global_store_dwordx4 v[136:137], v[242:245], off offset:576
	s_mov_b32 s2, 0x120000
	v_lshl_add_u64 v[164:165], v[158:159], 0, s[2:3]
	global_load_dwordx4 v[186:189], v[164:165], off
	global_load_dwordx4 v[194:197], v[164:165], off offset:64
	global_load_dwordx4 v[198:201], v[164:165], off offset:512
	global_load_dwordx4 v[242:245], v[164:165], off offset:576
	s_waitcnt vmcnt(16)
	v_pk_fma_f32 v[206:207], v[86:87], v[170:171], v[206:207]
	v_pk_fma_f32 v[204:205], v[84:85], v[168:169], v[204:205]
	v_pk_fma_f32 v[210:211], v[78:79], v[174:175], v[210:211]
	v_pk_fma_f32 v[208:209], v[76:77], v[172:173], v[208:209]
	v_pk_fma_f32 v[214:215], v[74:75], v[178:179], v[214:215]
	v_pk_fma_f32 v[212:213], v[72:73], v[176:177], v[212:213]
	v_pk_fma_f32 v[218:219], v[70:71], v[182:183], v[218:219]
	v_pk_fma_f32 v[216:217], v[68:69], v[180:181], v[216:217]
	s_mov_b32 s2, 0x60000
	v_lshl_add_u64 v[136:137], v[156:157], 0, s[2:3]
	global_store_dwordx4 v[136:137], v[204:207], off
	global_store_dwordx4 v[136:137], v[208:211], off offset:64
	global_store_dwordx4 v[136:137], v[212:215], off offset:512
	global_store_dwordx4 v[136:137], v[216:219], off offset:576
	s_mov_b32 s2, 0x140000
	v_lshl_add_u64 v[164:165], v[158:159], 0, s[2:3]
	global_load_dwordx4 v[204:207], v[164:165], off
	global_load_dwordx4 v[208:211], v[164:165], off offset:64
	global_load_dwordx4 v[212:215], v[164:165], off offset:512
	global_load_dwordx4 v[216:219], v[164:165], off offset:576
	s_waitcnt vmcnt(16)
	v_pk_fma_f32 v[228:229], v[66:67], v[170:171], v[228:229]
	v_pk_fma_f32 v[226:227], v[64:65], v[168:169], v[226:227]
	v_pk_fma_f32 v[232:233], v[62:63], v[174:175], v[232:233]
	v_pk_fma_f32 v[230:231], v[60:61], v[172:173], v[230:231]
	v_pk_fma_f32 v[236:237], v[58:59], v[178:179], v[236:237]
	v_pk_fma_f32 v[234:235], v[56:57], v[176:177], v[234:235]
	v_pk_fma_f32 v[240:241], v[50:51], v[182:183], v[240:241]
	v_pk_fma_f32 v[238:239], v[48:49], v[180:181], v[238:239]
	s_mov_b32 s2, 0x100000
	v_lshl_add_u64 v[136:137], v[156:157], 0, s[2:3]
	global_store_dwordx4 v[136:137], v[226:229], off
	global_store_dwordx4 v[136:137], v[230:233], off offset:64
	global_store_dwordx4 v[136:137], v[234:237], off offset:512
	global_store_dwordx4 v[136:137], v[238:241], off offset:576
	s_mov_b32 s2, 0x160000
	v_lshl_add_u64 v[164:165], v[158:159], 0, s[2:3]
	global_load_dwordx4 v[226:229], v[164:165], off
	global_load_dwordx4 v[230:233], v[164:165], off offset:64
	global_load_dwordx4 v[234:237], v[164:165], off offset:512
	global_load_dwordx4 v[238:241], v[164:165], off offset:576
	s_waitcnt vmcnt(16)
	v_pk_fma_f32 v[188:189], v[54:55], v[170:171], v[188:189]
	v_pk_fma_f32 v[186:187], v[52:53], v[168:169], v[186:187]
	v_pk_fma_f32 v[196:197], v[46:47], v[174:175], v[196:197]
	v_pk_fma_f32 v[194:195], v[44:45], v[172:173], v[194:195]
	v_pk_fma_f32 v[200:201], v[42:43], v[178:179], v[200:201]
	v_pk_fma_f32 v[198:199], v[40:41], v[176:177], v[198:199]
	v_pk_fma_f32 v[244:245], v[34:35], v[182:183], v[244:245]
	v_pk_fma_f32 v[242:243], v[32:33], v[180:181], v[242:243]
	s_mov_b32 s2, 0x120000
	v_lshl_add_u64 v[136:137], v[156:157], 0, s[2:3]
	global_store_dwordx4 v[136:137], v[186:189], off
	global_store_dwordx4 v[136:137], v[194:197], off offset:64
	global_store_dwordx4 v[136:137], v[198:201], off offset:512
	global_store_dwordx4 v[136:137], v[242:245], off offset:576
	s_waitcnt vmcnt(12)
	v_pk_fma_f32 v[206:207], v[38:39], v[170:171], v[206:207]
	v_pk_fma_f32 v[204:205], v[36:37], v[168:169], v[204:205]
	v_pk_fma_f32 v[210:211], v[30:31], v[174:175], v[210:211]
	v_pk_fma_f32 v[208:209], v[28:29], v[172:173], v[208:209]
	v_pk_fma_f32 v[214:215], v[26:27], v[178:179], v[214:215]
	v_pk_fma_f32 v[212:213], v[24:25], v[176:177], v[212:213]
	v_pk_fma_f32 v[218:219], v[18:19], v[182:183], v[218:219]
	v_pk_fma_f32 v[216:217], v[16:17], v[180:181], v[216:217]
	s_mov_b32 s2, 0x140000
	v_lshl_add_u64 v[136:137], v[156:157], 0, s[2:3]
	global_store_dwordx4 v[136:137], v[204:207], off
	global_store_dwordx4 v[136:137], v[208:211], off offset:64
	global_store_dwordx4 v[136:137], v[212:215], off offset:512
	global_store_dwordx4 v[136:137], v[216:219], off offset:576
	s_waitcnt vmcnt(8)
	v_pk_fma_f32 v[228:229], v[22:23], v[170:171], v[228:229]
	v_pk_fma_f32 v[226:227], v[20:21], v[168:169], v[226:227]
	v_pk_fma_f32 v[232:233], v[14:15], v[174:175], v[232:233]
	v_pk_fma_f32 v[230:231], v[12:13], v[172:173], v[230:231]
	v_pk_fma_f32 v[236:237], v[10:11], v[178:179], v[236:237]
	v_pk_fma_f32 v[234:235], v[8:9], v[176:177], v[234:235]
	v_pk_fma_f32 v[240:241], v[6:7], v[182:183], v[240:241]
	v_pk_fma_f32 v[238:239], v[4:5], v[180:181], v[238:239]
	s_mov_b32 s2, 0x160000
	v_lshl_add_u64 v[136:137], v[156:157], 0, s[2:3]
	global_store_dwordx4 v[136:137], v[226:229], off
	global_store_dwordx4 v[136:137], v[230:233], off offset:64
	global_store_dwordx4 v[136:137], v[234:237], off offset:512
	global_store_dwordx4 v[136:137], v[238:241], off offset:576
	s_mov_b64 s[4:5], -1
	s_andn2_b64 vcc, exec, s[44:45]
	s_cbranch_vccnz .LBB0_7139
	s_andn2_b64 vcc, exec, s[70:71]
	s_cbranch_vccnz .LBB0_7138
	s_barrier
	s_branch .LBB0_7138

.LBB0_9202:
	v_lshl_add_u32 v148, s44, 8, v1
	v_readlane_b32 s4, v254, 6
	v_ashrrev_i32_e32 v149, 31, v148
	v_readlane_b32 s5, v254, 7
	s_ashr_i32 s2, s42, 31
	s_lshr_b32 s2, s2, 29
	v_lshl_add_u64 v[144:145], v[148:149], 2, s[4:5]
	global_load_dword v154, v[144:145], off
	global_load_dword v170, v[144:145], off offset:64
	global_load_dword v172, v[144:145], off offset:128
	global_load_dword v174, v[144:145], off offset:192
	global_load_dword v176, v[144:145], off offset:512
	global_load_dword v178, v[144:145], off offset:576
	global_load_dword v180, v[144:145], off offset:640
	global_load_dword v182, v[144:145], off offset:704
	s_add_i32 s2, s42, s2
	s_and_b32 s2, s2, 0xfffff8
	s_sub_i32 s2, s42, s2
	v_lshl_or_b32 v142, s2, 8, v151
	v_readlane_b32 s2, v254, 4
	v_ashrrev_i32_e32 v143, 31, v142
	v_lshlrev_b64 v[146:147], 12, v[148:149]
	v_readlane_b32 s3, v254, 5
	s_waitcnt vmcnt(0)
	v_pk_mul_f32 v[130:131], v[130:131], v[154:155] op_sel_hi:[1,0]
	v_lshl_add_u64 v[156:157], s[2:3], 0, v[146:147]
	v_lshlrev_b64 v[146:147], 1, v[142:143]
	v_lshl_add_u64 v[142:143], v[156:157], 0, v[146:147]
	v_pk_mul_f32 v[128:129], v[128:129], v[154:155] op_sel_hi:[1,0]
	v_pk_mul_f32 v[156:157], v[126:127], v[154:155] op_sel_hi:[1,0]
	v_pk_mul_f32 v[126:127], v[124:125], v[154:155] op_sel_hi:[1,0]
	v_cvt_pk_bf16_f32 v124, v128, v129
	v_cvt_pk_bf16_f32 v125, v130, v131
	v_pk_mul_f32 v[120:121], v[120:121], v[154:155] op_sel_hi:[1,0]
	v_cvt_pk_bf16_f32 v126, v126, v127
	v_cvt_pk_bf16_f32 v127, v156, v157
	global_store_dwordx4 v[142:143], v[124:127], off
	v_pk_mul_f32 v[122:123], v[122:123], v[154:155] op_sel_hi:[1,0]
	s_nop 0
	v_pk_mul_f32 v[124:125], v[118:119], v[154:155] op_sel_hi:[1,0]
	v_pk_mul_f32 v[118:119], v[116:117], v[154:155] op_sel_hi:[1,0]
	v_cvt_pk_bf16_f32 v116, v120, v121
	v_cvt_pk_bf16_f32 v117, v122, v123
	s_nop 0
	v_cvt_pk_bf16_f32 v118, v118, v119
	v_cvt_pk_bf16_f32 v119, v124, v125
	global_store_dwordx4 v[142:143], v[116:119], off offset:256
	s_nop 1
	v_or_b32_e32 v116, 16, v148
	v_ashrrev_i32_e32 v117, 31, v116
	v_lshl_add_u64 v[118:119], v[116:117], 2, s[4:5]
	s_nop 1
	v_mov_b32_e32 v118, v170
	v_lshlrev_b64 v[116:117], 12, v[116:117]
	v_lshl_add_u64 v[116:117], s[2:3], 0, v[116:117]
	v_lshl_add_u64 v[116:117], v[116:117], 0, v[146:147]
	v_pk_mul_f32 v[114:115], v[114:115], v[118:119] op_sel_hi:[1,0]
	v_pk_mul_f32 v[112:113], v[112:113], v[118:119] op_sel_hi:[1,0]
	v_pk_mul_f32 v[120:121], v[110:111], v[118:119] op_sel_hi:[1,0]
	v_pk_mul_f32 v[110:111], v[108:109], v[118:119] op_sel_hi:[1,0]
	v_cvt_pk_bf16_f32 v108, v112, v113
	v_cvt_pk_bf16_f32 v109, v114, v115
	v_pk_mul_f32 v[104:105], v[104:105], v[118:119] op_sel_hi:[1,0]
	v_cvt_pk_bf16_f32 v110, v110, v111
	v_cvt_pk_bf16_f32 v111, v120, v121
	global_store_dwordx4 v[116:117], v[108:111], off
	v_pk_mul_f32 v[106:107], v[106:107], v[118:119] op_sel_hi:[1,0]
	s_nop 0
	v_pk_mul_f32 v[108:109], v[102:103], v[118:119] op_sel_hi:[1,0]
	v_pk_mul_f32 v[102:103], v[100:101], v[118:119] op_sel_hi:[1,0]
	v_cvt_pk_bf16_f32 v100, v104, v105
	v_cvt_pk_bf16_f32 v101, v106, v107
	s_nop 0
	v_cvt_pk_bf16_f32 v102, v102, v103
	v_cvt_pk_bf16_f32 v103, v108, v109
	global_store_dwordx4 v[116:117], v[100:103], off offset:256
	s_nop 1
	v_or_b32_e32 v100, 32, v148
	v_ashrrev_i32_e32 v101, 31, v100
	v_lshl_add_u64 v[102:103], v[100:101], 2, s[4:5]
	s_nop 1
	v_mov_b32_e32 v102, v172
	v_lshlrev_b64 v[100:101], 12, v[100:101]
	v_lshl_add_u64 v[100:101], s[2:3], 0, v[100:101]
	v_lshl_add_u64 v[100:101], v[100:101], 0, v[146:147]
	v_pk_mul_f32 v[98:99], v[98:99], v[102:103] op_sel_hi:[1,0]
	v_pk_mul_f32 v[96:97], v[96:97], v[102:103] op_sel_hi:[1,0]
	v_pk_mul_f32 v[104:105], v[94:95], v[102:103] op_sel_hi:[1,0]
	v_pk_mul_f32 v[94:95], v[92:93], v[102:103] op_sel_hi:[1,0]
	v_cvt_pk_bf16_f32 v92, v96, v97
	v_cvt_pk_bf16_f32 v93, v98, v99
	v_pk_mul_f32 v[88:89], v[88:89], v[102:103] op_sel_hi:[1,0]
	v_cvt_pk_bf16_f32 v94, v94, v95
	v_cvt_pk_bf16_f32 v95, v104, v105
	global_store_dwordx4 v[100:101], v[92:95], off
	v_pk_mul_f32 v[90:91], v[90:91], v[102:103] op_sel_hi:[1,0]
	s_nop 0
	v_pk_mul_f32 v[92:93], v[86:87], v[102:103] op_sel_hi:[1,0]
	v_pk_mul_f32 v[86:87], v[84:85], v[102:103] op_sel_hi:[1,0]
	v_cvt_pk_bf16_f32 v84, v88, v89
	v_cvt_pk_bf16_f32 v85, v90, v91
	s_nop 0
	v_cvt_pk_bf16_f32 v86, v86, v87
	v_cvt_pk_bf16_f32 v87, v92, v93
	global_store_dwordx4 v[100:101], v[84:87], off offset:256
	s_nop 1
	v_or_b32_e32 v84, 48, v148
	v_ashrrev_i32_e32 v85, 31, v84
	v_lshl_add_u64 v[86:87], v[84:85], 2, s[4:5]
	s_nop 1
	v_mov_b32_e32 v86, v174
	v_lshlrev_b64 v[84:85], 12, v[84:85]
	v_lshl_add_u64 v[84:85], s[2:3], 0, v[84:85]
	v_lshl_add_u64 v[84:85], v[84:85], 0, v[146:147]
	s_mov_b64 s[2:3], 0x80000
	s_mov_b64 s[4:5], -1
	v_pk_mul_f32 v[82:83], v[82:83], v[86:87] op_sel_hi:[1,0]
	v_pk_mul_f32 v[80:81], v[80:81], v[86:87] op_sel_hi:[1,0]
	v_pk_mul_f32 v[88:89], v[78:79], v[86:87] op_sel_hi:[1,0]
	v_pk_mul_f32 v[78:79], v[76:77], v[86:87] op_sel_hi:[1,0]
	v_cvt_pk_bf16_f32 v76, v80, v81
	v_cvt_pk_bf16_f32 v77, v82, v83
	v_pk_mul_f32 v[74:75], v[74:75], v[86:87] op_sel_hi:[1,0]
	v_cvt_pk_bf16_f32 v78, v78, v79
	v_cvt_pk_bf16_f32 v79, v88, v89
	global_store_dwordx4 v[84:85], v[76:79], off
	v_pk_mul_f32 v[72:73], v[72:73], v[86:87] op_sel_hi:[1,0]
	s_nop 0
	v_pk_mul_f32 v[76:77], v[70:71], v[86:87] op_sel_hi:[1,0]
	v_pk_mul_f32 v[70:71], v[68:69], v[86:87] op_sel_hi:[1,0]
	v_cvt_pk_bf16_f32 v68, v72, v73
	v_cvt_pk_bf16_f32 v69, v74, v75
	s_nop 0
	v_cvt_pk_bf16_f32 v70, v70, v71
	v_cvt_pk_bf16_f32 v71, v76, v77
	global_store_dwordx4 v[84:85], v[68:71], off offset:256
	s_nop 1
	v_mov_b32_e32 v68, v176
	v_pk_mul_f32 v[64:65], v[64:65], v[68:69] op_sel_hi:[1,0]
	v_lshl_add_u64 v[70:71], v[142:143], 0, s[2:3]
	s_mov_b32 s2, 0x80000
	v_pk_mul_f32 v[72:73], v[62:63], v[68:69] op_sel_hi:[1,0]
	v_pk_mul_f32 v[62:63], v[60:61], v[68:69] op_sel_hi:[1,0]
	v_cvt_pk_bf16_f32 v60, v64, v65
	v_add_co_u32_e32 v64, vcc, s2, v142
	v_pk_mul_f32 v[66:67], v[66:67], v[68:69] op_sel_hi:[1,0]
	s_nop 0
	v_addc_co_u32_e32 v65, vcc, 0, v143, vcc
	v_cvt_pk_bf16_f32 v61, v66, v67
	v_cvt_pk_bf16_f32 v62, v62, v63
	v_cvt_pk_bf16_f32 v63, v72, v73
	global_store_dwordx4 v[64:65], v[60:63], off
	v_pk_mul_f32 v[58:59], v[58:59], v[68:69] op_sel_hi:[1,0]
	v_pk_mul_f32 v[56:57], v[56:57], v[68:69] op_sel_hi:[1,0]
	v_pk_mul_f32 v[60:61], v[54:55], v[68:69] op_sel_hi:[1,0]
	v_pk_mul_f32 v[54:55], v[52:53], v[68:69] op_sel_hi:[1,0]
	v_cvt_pk_bf16_f32 v52, v56, v57
	v_cvt_pk_bf16_f32 v53, v58, v59
	s_mov_b64 s[2:3], 0x90000
	v_cvt_pk_bf16_f32 v54, v54, v55
	v_cvt_pk_bf16_f32 v55, v60, v61
	global_store_dwordx4 v[70:71], v[52:55], off offset:256
	s_nop 1
	v_mov_b32_e32 v52, v178
	v_pk_mul_f32 v[48:49], v[48:49], v[52:53] op_sel_hi:[1,0]
	v_lshl_add_u64 v[54:55], v[142:143], 0, s[2:3]
	s_mov_b32 s2, 0x90000
	v_pk_mul_f32 v[56:57], v[46:47], v[52:53] op_sel_hi:[1,0]
	v_pk_mul_f32 v[46:47], v[44:45], v[52:53] op_sel_hi:[1,0]
	v_cvt_pk_bf16_f32 v44, v48, v49
	v_add_co_u32_e32 v48, vcc, s2, v142
	v_pk_mul_f32 v[50:51], v[50:51], v[52:53] op_sel_hi:[1,0]
	s_nop 0
	v_addc_co_u32_e32 v49, vcc, 0, v143, vcc
	v_cvt_pk_bf16_f32 v45, v50, v51
	v_cvt_pk_bf16_f32 v46, v46, v47
	v_cvt_pk_bf16_f32 v47, v56, v57
	global_store_dwordx4 v[48:49], v[44:47], off
	v_pk_mul_f32 v[42:43], v[42:43], v[52:53] op_sel_hi:[1,0]
	v_pk_mul_f32 v[40:41], v[40:41], v[52:53] op_sel_hi:[1,0]
	v_pk_mul_f32 v[44:45], v[38:39], v[52:53] op_sel_hi:[1,0]
	v_pk_mul_f32 v[38:39], v[36:37], v[52:53] op_sel_hi:[1,0]
	v_cvt_pk_bf16_f32 v36, v40, v41
	v_cvt_pk_bf16_f32 v37, v42, v43
	s_mov_b64 s[2:3], 0xa0000
	v_cvt_pk_bf16_f32 v38, v38, v39
	v_cvt_pk_bf16_f32 v39, v44, v45
	global_store_dwordx4 v[54:55], v[36:39], off offset:256
	s_nop 1
	v_mov_b32_e32 v36, v180
	v_pk_mul_f32 v[32:33], v[32:33], v[36:37] op_sel_hi:[1,0]
	v_lshl_add_u64 v[38:39], v[142:143], 0, s[2:3]
	s_mov_b32 s2, 0xa0000
	v_pk_mul_f32 v[40:41], v[30:31], v[36:37] op_sel_hi:[1,0]
	v_pk_mul_f32 v[30:31], v[28:29], v[36:37] op_sel_hi:[1,0]
	v_cvt_pk_bf16_f32 v28, v32, v33
	v_add_co_u32_e32 v32, vcc, s2, v142
	v_pk_mul_f32 v[34:35], v[34:35], v[36:37] op_sel_hi:[1,0]
	s_nop 0
	v_addc_co_u32_e32 v33, vcc, 0, v143, vcc
	v_cvt_pk_bf16_f32 v29, v34, v35
	v_cvt_pk_bf16_f32 v30, v30, v31
	v_cvt_pk_bf16_f32 v31, v40, v41
	global_store_dwordx4 v[32:33], v[28:31], off
	v_pk_mul_f32 v[26:27], v[26:27], v[36:37] op_sel_hi:[1,0]
	v_pk_mul_f32 v[24:25], v[24:25], v[36:37] op_sel_hi:[1,0]
	v_pk_mul_f32 v[28:29], v[22:23], v[36:37] op_sel_hi:[1,0]
	v_pk_mul_f32 v[22:23], v[20:21], v[36:37] op_sel_hi:[1,0]
	v_cvt_pk_bf16_f32 v20, v24, v25
	v_cvt_pk_bf16_f32 v21, v26, v27
	s_mov_b64 s[2:3], 0xb0000
	v_cvt_pk_bf16_f32 v22, v22, v23
	v_cvt_pk_bf16_f32 v23, v28, v29
	global_store_dwordx4 v[38:39], v[20:23], off offset:256
	s_nop 1
	v_mov_b32_e32 v20, v182
	v_pk_mul_f32 v[16:17], v[16:17], v[20:21] op_sel_hi:[1,0]
	v_lshl_add_u64 v[22:23], v[142:143], 0, s[2:3]
	s_mov_b32 s2, 0xb0000
	v_pk_mul_f32 v[24:25], v[14:15], v[20:21] op_sel_hi:[1,0]
	v_pk_mul_f32 v[14:15], v[12:13], v[20:21] op_sel_hi:[1,0]
	v_cvt_pk_bf16_f32 v12, v16, v17
	v_add_co_u32_e32 v16, vcc, s2, v142
	v_pk_mul_f32 v[18:19], v[18:19], v[20:21] op_sel_hi:[1,0]
	s_nop 0
	v_addc_co_u32_e32 v17, vcc, 0, v143, vcc
	v_cvt_pk_bf16_f32 v13, v18, v19
	v_cvt_pk_bf16_f32 v14, v14, v15
	v_cvt_pk_bf16_f32 v15, v24, v25
	global_store_dwordx4 v[16:17], v[12:15], off
	s_andn2_b64 vcc, exec, s[40:41]
	v_pk_mul_f32 v[10:11], v[10:11], v[20:21] op_sel_hi:[1,0]
	v_pk_mul_f32 v[12:13], v[6:7], v[20:21] op_sel_hi:[1,0]
	v_pk_mul_f32 v[6:7], v[4:5], v[20:21] op_sel_hi:[1,0]
	v_pk_mul_f32 v[8:9], v[8:9], v[20:21] op_sel_hi:[1,0]
	s_nop 0
	v_cvt_pk_bf16_f32 v4, v8, v9
	v_cvt_pk_bf16_f32 v5, v10, v11
	v_cvt_pk_bf16_f32 v6, v6, v7
	v_cvt_pk_bf16_f32 v7, v12, v13
	global_store_dwordx4 v[22:23], v[4:7], off offset:256
	s_cbranch_vccnz .LBB0_9195
	s_andn2_b64 vcc, exec, s[0:1]
	s_cbranch_vccnz .LBB0_9194
	s_barrier
	s_branch .LBB0_9194
